# mLSTM chunk loop: counted vmcnt at chunk-end barrier (weight DMA and h stores stay in flight), removed store-ack waits
# speedup vs baseline: 1.0036x; 1.0036x over previous
.LBB0_682:
	s_lshl_b32 s0, s39, 7
	s_lshl_b32 s1, s0, 2
	v_readlane_b32 s2, v243, 19
	s_add_u32 s1, s2, s1
	v_readlane_b32 s2, v243, 20
	s_addc_u32 s3, s2, 0
	s_lshl_b32 s2, s47, 2
	s_add_u32 s2, s1, s2
	s_addc_u32 s3, s3, 0
	s_lshl_b32 s34, s0, 1
	v_mov_b32_e32 v139, v115
	v_mov_b32_e32 v26, 0
	s_lshl_b32 s46, s46, 11
	s_mov_b32 s47, 1
	v_lshl_add_u64 v[144:145], v[120:121], 0, s[34:35]
	s_mul_i32 s30, s38, 0x4800
	s_mov_b32 s31, s35
	v_lshl_add_u64 v[146:147], s[2:3], 0, v[138:139]
	v_lshl_add_u64 v[148:149], v[134:135], 0, s[34:35]
	s_mov_b32 s48, 0
	s_movk_i32 s49, 0xff80
	v_mov_b32_e32 v139, v181
	v_readlane_b32 s50, v242, 25
	v_readlane_b32 s51, v242, 10
	v_mov_b32_e32 v27, v26
	v_mov_b32_e32 v28, v26
	v_mov_b32_e32 v29, v26
	v_mov_b32_e32 v30, v26
	v_mov_b32_e32 v31, v26
	v_mov_b32_e32 v32, v26
	v_mov_b32_e32 v33, v26
	v_mov_b32_e32 v34, v26
	v_mov_b32_e32 v35, v26
	v_mov_b32_e32 v36, v26
	v_mov_b32_e32 v37, v26
	s_waitcnt vmcnt(0)
	s_branch .LBB0_685

.LBB0_684:
	s_nop 4
	v_cvt_pk_f16_f32 v39, v32, v33
	v_cvt_pk_f16_f32 v38, v30, v31
	s_waitcnt lgkmcnt(0)
	s_cmp_eq_u32 s99, 0
	s_cbranch_scc1 .Lml0_nodma
	s_waitcnt vmcnt(10)
	s_branch .Lml0_join
.Lml0_nodma:
	s_waitcnt vmcnt(2)
.Lml0_join:
	s_barrier
	ds_write_b64 v186, v[38:39] offset:49152
	v_cvt_pk_f16_f32 v39, v36, v37
	v_cvt_pk_f16_f32 v38, v34, v35
	ds_write_b64 v186, v[38:39] offset:53504
	v_cvt_pk_f16_f32 v39, v28, v29
	v_cvt_pk_f16_f32 v38, v26, v27
	ds_write_b64 v186, v[38:39] offset:57856
	s_addk_i32 s48, 0x80
	s_add_i32 s51, s51, s33
	s_add_i32 s50, s50, s41
	s_add_i32 s47, s47, 1
	s_addk_i32 s49, 0xff80
	v_mov_b64_e32 v[38:39], v[62:63]
	v_mov_b64_e32 v[42:43], v[58:59]
	v_mov_b64_e32 v[46:47], v[54:55]
	v_mov_b64_e32 v[68:69], v[52:53]
	v_add_u32_e32 v139, 0x200, v139
	s_cmpk_eq_i32 s48, 0x900
	v_mov_b64_e32 v[40:41], v[64:65]
	v_mov_b64_e32 v[44:45], v[60:61]
	v_mov_b64_e32 v[48:49], v[56:57]
	v_mov_b64_e32 v[66:67], v[50:51]
	s_cbranch_scc1 .LBB0_814
.LBB0_685:
	s_mov_b32 s99, 0
	s_cmp_eq_u32 s48, 0
	s_cselect_b64 s[0:1], -1, 0
	s_or_b64 s[0:1], s[28:29], s[0:1]
	v_add_u32_e32 v50, v110, v118
	s_and_b64 vcc, exec, s[0:1]
	ds_write_b128 v185, v[6:9]
	ds_write_b128 v185, v[10:13] offset:64
	ds_write_b128 v185, v[14:17] offset:128
	ds_write_b128 v185, v[18:21] offset:192
	ds_write_b128 v50, v[22:25] offset:34816
	s_waitcnt lgkmcnt(0)
	s_barrier
	s_cbranch_vccnz .LBB0_693
	s_add_i32 s36, s40, s51
	s_cmpk_gt_i32 s36, 0x47ff
	s_cbranch_scc1 .LBB0_693
	s_mul_hi_i32 s0, s36, 0x30c30c31
	s_lshr_b32 s1, s0, 31
	s_ashr_i32 s3, s0, 10
	s_add_i32 s3, s3, s1
	s_waitcnt vmcnt(2)
	s_mul_i32 s0, s3, 0xffffeb00
	s_add_i32 s36, s36, s0
	s_cmpk_gt_i32 s36, 0xdff
	s_mov_b64 s[0:1], -1
	s_cbranch_scc0 .LBB0_689
	v_readlane_b32 s1, v242, 24
	s_mul_i32 s0, s3, 0xffffd600
	s_add_i32 s1, s1, s50
	s_add_i32 s1, s1, s0
	s_and_b32 s2, s1, 0x7fffffc0
	s_mov_b64 s[0:1], 0

.LBB0_693:
	s_cmpk_eq_i32 s48, 0x880
	s_cselect_b64 s[36:37], -1, 0
	v_mov_b64_e32 v[50:51], v[66:67]
	v_mov_b64_e32 v[56:57], v[48:49]
	v_mov_b64_e32 v[60:61], v[44:45]
	v_mov_b64_e32 v[64:65], v[40:41]
	s_and_b64 vcc, exec, s[36:37]
	v_mov_b64_e32 v[52:53], v[68:69]
	v_mov_b64_e32 v[54:55], v[46:47]
	v_mov_b64_e32 v[58:59], v[42:43]
	v_mov_b64_e32 v[62:63], v[38:39]
	s_cbranch_vccnz .LBB0_700
	s_cmp_lg_u32 s48, 0
	v_add_u32_e32 v6, s49, v182
	s_cbranch_scc0 .LBB0_696
	v_add_u32_e32 v7, s48, v123
	v_add_u32_e32 v7, 0xffffff80, v7
	v_add_u32_e32 v8, 0x8ff, v6
	v_cndmask_b32_e64 v7, v8, v7, s[86:87]
	v_add_u32_e32 v22, s46, v7
	s_mov_b64 s[0:1], 0
	s_branch .LBB0_697

.LBB0_754:
	s_bitcmp1_b32 s55, 7
	s_cselect_b64 s[80:81], -1, 0
	s_and_b64 s[80:81], s[0:1], s[80:81]
	s_and_b64 s[80:81], s[80:81], exec
	s_cselect_b32 s2, s38, s2
	s_cselect_b32 s3, s39, s3
	v_mov_b32_e32 v78, s2
	s_ashr_i32 s2, s55, 1
	s_and_b32 s2, s2, 0xffffff80
	v_bitop3_b32 v81, s55, v192, v163 bitop3:0xc8
	v_or_b32_e32 v80, s55, v163
	v_or_b32_e32 v81, s2, v81
	v_or_b32_e32 v86, s54, v158
	v_mov_b32_e32 v79, s3
	v_cndmask_b32_e64 v80, v80, v81, s[0:1]
	v_mad_i64_i32 v[86:87], s[0:1], s96, v86, 0
	v_readlane_b32 s53, v242, 36
	v_ashrrev_i32_e32 v81, 31, v80
	v_lshl_add_u64 v[78:79], v[86:87], 2, v[78:79]
	s_mov_b32 m0, s53
	v_lshl_add_u64 v[78:79], v[80:81], 2, v[78:79]
	s_lshl_b32 s0, s96, 5
	s_mov_b32 s1, s35
	global_load_lds_dwordx4 v[78:79], off nt
	v_lshl_add_u64 v[78:79], v[78:79], 0, s[0:1]
	s_add_i32 m0, s53, 0x410
	v_readlane_b32 s2, v242, 30
	global_load_lds_dwordx4 v[78:79], off nt
	v_lshl_add_u64 v[78:79], v[78:79], 0, s[0:1]
	s_mov_b32 m0, s2
	v_readlane_b32 s2, v242, 31
	global_load_lds_dwordx4 v[78:79], off nt
	v_lshl_add_u64 v[78:79], v[78:79], 0, s[0:1]
	s_mov_b32 m0, s2
	v_readlane_b32 s2, v242, 33
	global_load_lds_dwordx4 v[78:79], off nt
	v_lshl_add_u64 v[78:79], v[78:79], 0, s[0:1]
	s_mov_b32 m0, s2
	v_readlane_b32 s2, v242, 34
	global_load_lds_dwordx4 v[78:79], off nt
	v_lshl_add_u64 v[78:79], v[78:79], 0, s[0:1]
	s_mov_b32 m0, s2
	v_readlane_b32 s2, v242, 35
	global_load_lds_dwordx4 v[78:79], off nt
	v_lshl_add_u64 v[78:79], v[78:79], 0, s[0:1]
	s_mov_b32 m0, s2
	s_nop 0
	global_load_lds_dwordx4 v[78:79], off nt
	v_lshl_add_u64 v[78:79], v[78:79], 0, s[0:1]
	v_readlane_b32 s0, v242, 38
	s_mov_b32 m0, s0
	s_nop 0
	global_load_lds_dwordx4 v[78:79], off nt
	s_mov_b32 s99, 1

.LBB0_2082:
	v_writelane_b32 v243, s54, 21
	s_lshl_b32 s0, s39, 7
	s_lshl_b32 s1, s0, 2
	v_readlane_b32 s2, v243, 29
	s_add_u32 s1, s2, s1
	v_readlane_b32 s2, v242, 25
	s_addc_u32 s3, s2, 0
	s_lshl_b32 s2, s41, 2
	s_add_u32 s2, s1, s2
	s_addc_u32 s3, s3, 0
	s_lshl_b32 s30, s0, 1
	v_mov_b32_e32 v135, v111
	v_mov_b32_e32 v26, 0
	s_lshl_b32 s51, s40, 11
	s_mov_b32 s52, 1
	v_lshl_add_u64 v[140:141], v[116:117], 0, s[30:31]
	s_mul_i32 s34, s38, 0x4800
	s_mov_b32 s35, s31
	v_lshl_add_u64 v[142:143], s[2:3], 0, v[134:135]
	v_lshl_add_u64 v[144:145], v[130:131], 0, s[30:31]
	s_mov_b32 s53, 0
	v_mov_b32_e32 v135, v177
	v_readlane_b32 s54, v243, 16
	s_mov_b32 s55, 0
	v_mov_b32_e32 v27, v26
	v_mov_b32_e32 v28, v26
	v_mov_b32_e32 v29, v26
	v_mov_b32_e32 v30, v26
	v_mov_b32_e32 v31, v26
	v_mov_b32_e32 v32, v26
	v_mov_b32_e32 v33, v26
	v_mov_b32_e32 v34, v26
	v_mov_b32_e32 v35, v26
	v_mov_b32_e32 v36, v26
	v_mov_b32_e32 v37, v26
	s_waitcnt vmcnt(0)
	s_branch .LBB0_2085

.Lml1_join:
	s_barrier
	ds_write_b64 v182, v[38:39] offset:49152
	v_cvt_pk_f16_f32 v39, v36, v37
	v_cvt_pk_f16_f32 v38, v34, v35
	ds_write_b64 v182, v[38:39] offset:53504
	v_cvt_pk_f16_f32 v39, v28, v29
	v_cvt_pk_f16_f32 v38, v26, v27
	ds_write_b64 v182, v[38:39] offset:57856
	s_addk_i32 s55, 0x80
	s_add_i32 s54, s54, s44
	s_add_i32 s52, s52, 1
	s_addk_i32 s53, 0xff80
	v_mov_b64_e32 v[38:39], v[62:63]
	v_mov_b64_e32 v[42:43], v[58:59]
	v_mov_b64_e32 v[46:47], v[54:55]
	v_mov_b64_e32 v[68:69], v[52:53]
	v_add_u32_e32 v135, 0x200, v135
	s_cmpk_eq_i32 s55, 0x900
	v_mov_b64_e32 v[40:41], v[64:65]
	v_mov_b64_e32 v[44:45], v[60:61]
	v_mov_b64_e32 v[48:49], v[56:57]
	v_mov_b64_e32 v[66:67], v[50:51]
	s_cbranch_scc1 .LBB0_2226
.LBB0_2085:
	s_mov_b32 s99, 0
	s_cmp_eq_u32 s55, 0
	s_cselect_b64 s[0:1], -1, 0
	s_or_b64 s[0:1], s[28:29], s[0:1]
	v_add_u32_e32 v50, v106, v114
	s_and_b64 vcc, exec, s[0:1]
	ds_write_b128 v181, v[6:9]
	ds_write_b128 v181, v[10:13] offset:64
	ds_write_b128 v181, v[14:17] offset:128
	ds_write_b128 v181, v[18:21] offset:192
	ds_write_b128 v50, v[22:25] offset:34816
	s_waitcnt lgkmcnt(0)
	s_barrier
	s_cbranch_vccnz .LBB0_2093
	s_add_i32 s12, s46, s54
	s_cmp_ge_i32 s12, s42
	s_cbranch_scc1 .LBB0_2093
	s_cmp_ge_i32 s12, s33
	s_cselect_b64 s[0:1], -1, 0
	s_and_b64 s[2:3], s[0:1], exec
	s_cselect_b32 s2, s45, s33
	s_add_i32 s13, s46, s2
	s_add_i32 s13, s13, s54
	v_readlane_b32 s36, v242, 27
	v_readlane_b32 s37, v242, 28
	s_mul_hi_i32 s3, s13, 0x30c30c31
	s_or_b64 s[0:1], s[36:37], s[0:1]
	s_lshr_b32 s9, s3, 31
	s_ashr_i32 s37, s3, 10
	s_add_i32 s37, s37, s9
	s_mul_i32 s3, s37, 0x1500
	s_waitcnt vmcnt(2)
	s_sub_i32 s2, s2, s3
	s_add_i32 s12, s12, s2
	s_cmpk_gt_i32 s12, 0xdff
	s_mov_b64 s[38:39], -1
	s_cbranch_scc0 .LBB0_2089
	s_and_b64 s[2:3], s[0:1], exec
	s_mov_b32 s2, 0xc600000
	s_cselect_b32 s2, s2, 0x8000000
	s_lshl_b32 s9, s12, 1
	s_add_i32 s9, s9, 0x7fffe400
	s_and_b32 s36, s9, 0x7fffffc0
	s_lshl_b32 s9, s13, 5
	s_mov_b32 s3, s31
	s_and_b32 s9, s9, 0x3e0
	s_mov_b64 s[38:39], 0

.LBB0_2093:
	s_cmpk_eq_i32 s55, 0x880
	s_cselect_b64 s[36:37], -1, 0
	v_mov_b64_e32 v[50:51], v[66:67]
	v_mov_b64_e32 v[56:57], v[48:49]
	v_mov_b64_e32 v[60:61], v[44:45]
	v_mov_b64_e32 v[64:65], v[40:41]
	s_and_b64 vcc, exec, s[36:37]
	v_mov_b64_e32 v[52:53], v[68:69]
	v_mov_b64_e32 v[54:55], v[46:47]
	v_mov_b64_e32 v[58:59], v[42:43]
	v_mov_b64_e32 v[62:63], v[38:39]
	s_cbranch_vccnz .LBB0_2100
	s_cmp_lg_u32 s55, 0
	v_add_u32_e32 v6, s53, v178
	s_cbranch_scc0 .LBB0_2096
	v_add_u32_e32 v7, s55, v119
	v_add_u32_e32 v7, 0xffffff80, v7
	v_add_u32_e32 v8, 0x87f, v6
	v_cndmask_b32_e64 v7, v8, v7, s[86:87]
	v_add_u32_e32 v22, s51, v7
	s_mov_b64 s[0:1], 0
	s_branch .LBB0_2097

.LBB0_2166:
	s_bitcmp1_b32 s12, 7
	s_cselect_b64 s[2:3], -1, 0
	s_and_b64 s[2:3], s[0:1], s[2:3]
	s_and_b64 s[2:3], s[2:3], exec
	s_cselect_b32 s2, s97, s41
	s_cselect_b32 s3, s96, s40
	v_mov_b32_e32 v87, s2
	s_ashr_i32 s2, s12, 1
	s_and_b32 s2, s2, 0xffffff80
	v_bitop3_b32 v89, s12, v188, v159 bitop3:0xc8
	v_or_b32_e32 v88, s12, v159
	v_or_b32_e32 v89, s2, v89
	v_or_b32_e32 v90, s59, v154
	v_mov_b32_e32 v86, s3
	v_cndmask_b32_e64 v88, v88, v89, s[0:1]
	v_mad_i64_i32 v[90:91], s[0:1], s38, v90, 0
	v_ashrrev_i32_e32 v89, 31, v88
	v_lshl_add_u64 v[86:87], v[90:91], 2, v[86:87]
	s_mov_b32 m0, s43
	v_lshl_add_u64 v[86:87], v[88:89], 2, v[86:87]
	s_lshl_b32 s0, s38, 5
	s_mov_b32 s1, s31
	global_load_lds_dwordx4 v[86:87], off nt
	v_lshl_add_u64 v[86:87], v[86:87], 0, s[0:1]
	s_add_i32 m0, s43, 0x410
	v_readlane_b32 s2, v242, 31
	global_load_lds_dwordx4 v[86:87], off nt
	v_lshl_add_u64 v[86:87], v[86:87], 0, s[0:1]
	s_mov_b32 m0, s2
	v_readlane_b32 s2, v242, 33
	global_load_lds_dwordx4 v[86:87], off nt
	v_lshl_add_u64 v[86:87], v[86:87], 0, s[0:1]
	s_mov_b32 m0, s2
	v_readlane_b32 s2, v242, 34
	global_load_lds_dwordx4 v[86:87], off nt
	v_lshl_add_u64 v[86:87], v[86:87], 0, s[0:1]
	s_mov_b32 m0, s2
	v_readlane_b32 s2, v242, 35
	global_load_lds_dwordx4 v[86:87], off nt
	v_lshl_add_u64 v[86:87], v[86:87], 0, s[0:1]
	s_mov_b32 m0, s2
	v_readlane_b32 s2, v242, 38
	global_load_lds_dwordx4 v[86:87], off nt
	v_lshl_add_u64 v[86:87], v[86:87], 0, s[0:1]
	s_mov_b32 m0, s2
	s_nop 0
	global_load_lds_dwordx4 v[86:87], off nt
	v_lshl_add_u64 v[86:87], v[86:87], 0, s[0:1]
	v_readlane_b32 s0, v242, 24
	s_mov_b32 m0, s0
	s_nop 0
	global_load_lds_dwordx4 v[86:87], off nt
	s_mov_b32 s99, 1

.LBB0_3699:
	v_writelane_b32 v243, s52, 25
	s_lshl_b32 s0, s39, 7
	s_lshl_b32 s1, s0, 2
	v_readlane_b32 s2, v243, 16
	s_add_u32 s1, s2, s1
	v_readlane_b32 s2, v243, 17
	s_addc_u32 s3, s2, 0
	s_lshl_b32 s2, s41, 2
	s_add_u32 s2, s1, s2
	s_addc_u32 s3, s3, 0
	s_lshl_b32 s34, s0, 1
	v_mov_b32_e32 v135, v111
	v_mov_b32_e32 v26, 0
	s_lshl_b32 s48, s40, 11
	s_mov_b32 s49, 1
	v_lshl_add_u64 v[140:141], v[116:117], 0, s[34:35]
	s_mul_i32 s30, s38, 0x4800
	s_mov_b32 s31, s35
	v_lshl_add_u64 v[142:143], s[2:3], 0, v[134:135]
	v_lshl_add_u64 v[144:145], v[130:131], 0, s[34:35]
	s_mov_b32 s50, 0
	s_movk_i32 s51, 0xff80
	v_mov_b32_e32 v135, v177
	v_readlane_b32 s52, v242, 51
	v_readlane_b32 s53, v242, 19
	v_mov_b32_e32 v27, v26
	v_mov_b32_e32 v28, v26
	v_mov_b32_e32 v29, v26
	v_mov_b32_e32 v30, v26
	v_mov_b32_e32 v31, v26
	v_mov_b32_e32 v32, v26
	v_mov_b32_e32 v33, v26
	v_mov_b32_e32 v34, v26
	v_mov_b32_e32 v35, v26
	v_mov_b32_e32 v36, v26
	v_mov_b32_e32 v37, v26
	s_waitcnt vmcnt(0)
	s_branch .LBB0_3702

.Lml2_join:
	s_barrier
	ds_write_b64 v182, v[38:39] offset:49152
	v_cvt_pk_f16_f32 v39, v36, v37
	v_cvt_pk_f16_f32 v38, v34, v35
	ds_write_b64 v182, v[38:39] offset:53504
	v_cvt_pk_f16_f32 v39, v28, v29
	v_cvt_pk_f16_f32 v38, v26, v27
	ds_write_b64 v182, v[38:39] offset:57856
	s_addk_i32 s50, 0x80
	s_add_i32 s53, s53, s33
	s_add_i32 s52, s52, s43
	s_add_i32 s49, s49, 1
	s_addk_i32 s51, 0xff80
	v_mov_b64_e32 v[38:39], v[62:63]
	v_mov_b64_e32 v[42:43], v[58:59]
	v_mov_b64_e32 v[46:47], v[54:55]
	v_mov_b64_e32 v[68:69], v[52:53]
	v_add_u32_e32 v135, 0x200, v135
	s_cmpk_eq_i32 s50, 0x900
	v_mov_b64_e32 v[40:41], v[64:65]
	v_mov_b64_e32 v[44:45], v[60:61]
	v_mov_b64_e32 v[48:49], v[56:57]
	v_mov_b64_e32 v[66:67], v[50:51]
	s_cbranch_scc1 .LBB0_3843
.LBB0_3702:
	s_mov_b32 s99, 0
	s_cmp_eq_u32 s50, 0
	s_cselect_b64 s[0:1], -1, 0
	s_or_b64 s[0:1], s[28:29], s[0:1]
	v_add_u32_e32 v50, v106, v114
	s_and_b64 vcc, exec, s[0:1]
	ds_write_b128 v181, v[6:9]
	ds_write_b128 v181, v[10:13] offset:64
	ds_write_b128 v181, v[14:17] offset:128
	ds_write_b128 v181, v[18:21] offset:192
	ds_write_b128 v50, v[22:25] offset:34816
	s_waitcnt lgkmcnt(0)
	s_barrier
	s_cbranch_vccnz .LBB0_3710
	s_add_i32 s36, s42, s53
	s_cmpk_gt_i32 s36, 0x47ff
	s_cbranch_scc1 .LBB0_3710
	s_mul_hi_i32 s0, s36, 0x30c30c31
	s_lshr_b32 s1, s0, 31
	s_ashr_i32 s3, s0, 10
	s_add_i32 s3, s3, s1
	s_waitcnt vmcnt(2)
	s_mul_i32 s0, s3, 0xffffeb00
	s_add_i32 s36, s36, s0
	s_cmpk_gt_i32 s36, 0xdff
	s_mov_b64 s[0:1], -1
	s_cbranch_scc0 .LBB0_3706
	v_readlane_b32 s1, v242, 23
	s_mul_i32 s0, s3, 0xffffd600
	s_add_i32 s1, s1, s52
	s_add_i32 s1, s1, s0
	s_and_b32 s2, s1, 0x7fffffc0
	s_mov_b64 s[0:1], 0

.LBB0_3710:
	s_cmpk_eq_i32 s50, 0x880
	s_cselect_b64 s[36:37], -1, 0
	v_mov_b64_e32 v[50:51], v[66:67]
	v_mov_b64_e32 v[56:57], v[48:49]
	v_mov_b64_e32 v[60:61], v[44:45]
	v_mov_b64_e32 v[64:65], v[40:41]
	s_and_b64 vcc, exec, s[36:37]
	v_mov_b64_e32 v[52:53], v[68:69]
	v_mov_b64_e32 v[54:55], v[46:47]
	v_mov_b64_e32 v[58:59], v[42:43]
	v_mov_b64_e32 v[62:63], v[38:39]
	s_cbranch_vccnz .LBB0_3717
	s_cmp_lg_u32 s50, 0
	v_add_u32_e32 v6, s51, v178
	s_cbranch_scc0 .LBB0_3713
	v_add_u32_e32 v7, s50, v119
	v_add_u32_e32 v7, 0xffffff80, v7
	v_add_u32_e32 v8, 0x8ff, v6
	v_cndmask_b32_e64 v7, v8, v7, s[86:87]
	v_add_u32_e32 v22, s48, v7
	s_mov_b64 s[0:1], 0
	s_branch .LBB0_3714

.LBB0_3783:
	s_bitcmp1_b32 s57, 7
	s_cselect_b64 s[2:3], -1, 0
	s_and_b64 s[2:3], s[0:1], s[2:3]
	s_and_b64 s[2:3], s[2:3], exec
	s_cselect_b32 s2, s97, s41
	s_cselect_b32 s3, s96, s40
	v_mov_b32_e32 v87, s2
	s_ashr_i32 s2, s57, 1
	s_and_b32 s2, s2, 0xffffff80
	v_bitop3_b32 v89, s57, v188, v159 bitop3:0xc8
	v_or_b32_e32 v88, s57, v159
	v_or_b32_e32 v89, s2, v89
	v_or_b32_e32 v90, s56, v154
	v_mov_b32_e32 v86, s3
	v_cndmask_b32_e64 v88, v88, v89, s[0:1]
	v_mad_i64_i32 v[90:91], s[0:1], s38, v90, 0
	v_readlane_b32 s39, v242, 7
	v_ashrrev_i32_e32 v89, 31, v88
	v_lshl_add_u64 v[86:87], v[90:91], 2, v[86:87]
	s_mov_b32 m0, s39
	v_lshl_add_u64 v[86:87], v[88:89], 2, v[86:87]
	s_lshl_b32 s0, s38, 5
	s_mov_b32 s1, s35
	global_load_lds_dwordx4 v[86:87], off nt
	v_lshl_add_u64 v[86:87], v[86:87], 0, s[0:1]
	s_add_i32 m0, s39, 0x410
	v_readlane_b32 s2, v242, 34
	global_load_lds_dwordx4 v[86:87], off nt
	v_lshl_add_u64 v[86:87], v[86:87], 0, s[0:1]
	s_mov_b32 m0, s2
	v_readlane_b32 s2, v242, 35
	global_load_lds_dwordx4 v[86:87], off nt
	v_lshl_add_u64 v[86:87], v[86:87], 0, s[0:1]
	s_mov_b32 m0, s2
	v_readlane_b32 s2, v242, 38
	global_load_lds_dwordx4 v[86:87], off nt
	v_lshl_add_u64 v[86:87], v[86:87], 0, s[0:1]
	s_mov_b32 m0, s2
	v_readlane_b32 s2, v242, 24
	global_load_lds_dwordx4 v[86:87], off nt
	v_lshl_add_u64 v[86:87], v[86:87], 0, s[0:1]
	s_mov_b32 m0, s2
	v_readlane_b32 s2, v242, 27
	global_load_lds_dwordx4 v[86:87], off nt
	v_lshl_add_u64 v[86:87], v[86:87], 0, s[0:1]
	s_mov_b32 m0, s2
	s_movk_i32 s55, 0x3000
	global_load_lds_dwordx4 v[86:87], off nt
	v_lshl_add_u64 v[86:87], v[86:87], 0, s[0:1]
	v_readlane_b32 s0, v242, 29
	s_mov_b32 m0, s0
	s_nop 0
	global_load_lds_dwordx4 v[86:87], off nt
	s_mov_b32 s99, 1

.LBB0_5062:
	v_writelane_b32 v243, s50, 25
	s_lshl_b32 s2, s39, 7
	s_lshl_b32 s3, s2, 2
	v_readlane_b32 s28, v243, 16
	s_add_u32 s3, s28, s3
	v_readlane_b32 s28, v243, 17
	s_addc_u32 s28, s28, 0
	s_lshl_b32 s29, s47, 2
	s_add_u32 s34, s3, s29
	s_addc_u32 s35, s28, 0
	s_lshl_b32 s30, s2, 1
	v_mov_b32_e32 v135, v111
	v_mov_b32_e32 v26, 0
	s_lshl_b32 s46, s46, 11
	s_mov_b32 s47, 1
	v_lshl_add_u64 v[140:141], v[116:117], 0, s[30:31]
	s_mul_i32 s28, s38, 0x4800
	s_mov_b32 s29, s31
	v_lshl_add_u64 v[142:143], s[34:35], 0, v[134:135]
	v_lshl_add_u64 v[144:145], v[130:131], 0, s[30:31]
	s_mov_b32 s48, 0
	s_movk_i32 s49, 0xff80
	v_mov_b32_e32 v135, v177
	v_readlane_b32 s50, v242, 51
	v_readlane_b32 s51, v242, 19
	v_mov_b32_e32 v27, v26
	v_mov_b32_e32 v28, v26
	v_mov_b32_e32 v29, v26
	v_mov_b32_e32 v30, v26
	v_mov_b32_e32 v31, v26
	v_mov_b32_e32 v32, v26
	v_mov_b32_e32 v33, v26
	v_mov_b32_e32 v34, v26
	v_mov_b32_e32 v35, v26
	v_mov_b32_e32 v36, v26
	v_mov_b32_e32 v37, v26
	s_waitcnt vmcnt(0)
	s_branch .LBB0_5065

.Lml3_join:
	s_barrier
	ds_write_b64 v182, v[38:39] offset:49152
	v_cvt_pk_f16_f32 v39, v36, v37
	v_cvt_pk_f16_f32 v38, v34, v35
	ds_write_b64 v182, v[38:39] offset:53504
	v_cvt_pk_f16_f32 v39, v28, v29
	v_cvt_pk_f16_f32 v38, v26, v27
	ds_write_b64 v182, v[38:39] offset:57856
	s_addk_i32 s48, 0x80
	s_add_i32 s51, s51, s33
	s_add_i32 s50, s50, s41
	s_add_i32 s47, s47, 1
	s_addk_i32 s49, 0xff80
	v_mov_b64_e32 v[38:39], v[62:63]
	v_mov_b64_e32 v[42:43], v[58:59]
	v_mov_b64_e32 v[46:47], v[54:55]
	v_mov_b64_e32 v[68:69], v[52:53]
	v_add_u32_e32 v135, 0x200, v135
	s_cmpk_eq_i32 s48, 0x900
	v_mov_b64_e32 v[40:41], v[64:65]
	v_mov_b64_e32 v[44:45], v[60:61]
	v_mov_b64_e32 v[48:49], v[56:57]
	v_mov_b64_e32 v[66:67], v[50:51]
	s_cbranch_scc1 .LBB0_5206
.LBB0_5065:
	s_mov_b32 s99, 0
	s_cmp_eq_u32 s48, 0
	s_cselect_b64 s[2:3], -1, 0
	s_or_b64 s[2:3], s[26:27], s[2:3]
	v_add_u32_e32 v50, v106, v114
	s_and_b64 vcc, exec, s[2:3]
	ds_write_b128 v181, v[6:9]
	ds_write_b128 v181, v[10:13] offset:64
	ds_write_b128 v181, v[14:17] offset:128
	ds_write_b128 v181, v[18:21] offset:192
	ds_write_b128 v50, v[22:25] offset:34816
	s_waitcnt lgkmcnt(0)
	s_barrier
	s_cbranch_vccnz .LBB0_5073
	s_add_i32 s2, s40, s51
	s_cmpk_gt_i32 s2, 0x47ff
	s_cbranch_scc1 .LBB0_5073
	s_add_i32 s36, s2, 0x4800
	s_mul_hi_i32 s2, s36, 0x30c30c31
	s_lshr_b32 s3, s2, 31
	s_ashr_i32 s35, s2, 10
	s_add_i32 s35, s35, s3
	s_waitcnt vmcnt(2)
	s_mul_i32 s2, s35, 0xffffeb00
	s_add_i32 s36, s36, s2
	s_cmpk_gt_i32 s36, 0xdff
	s_mov_b64 s[2:3], -1
	s_cbranch_scc0 .LBB0_5069
	v_readlane_b32 s3, v242, 23
	s_mul_i32 s2, s35, 0xffffd600
	s_add_i32 s3, s3, s50
	s_add_i32 s3, s3, s2
	s_and_b32 s34, s3, 0x7fffffc0
	s_mov_b64 s[2:3], 0

.LBB0_5073:
	s_cmpk_eq_i32 s48, 0x880
	s_cselect_b64 s[34:35], -1, 0
	v_mov_b64_e32 v[50:51], v[66:67]
	v_mov_b64_e32 v[56:57], v[48:49]
	v_mov_b64_e32 v[60:61], v[44:45]
	v_mov_b64_e32 v[64:65], v[40:41]
	s_and_b64 vcc, exec, s[34:35]
	v_mov_b64_e32 v[52:53], v[68:69]
	v_mov_b64_e32 v[54:55], v[46:47]
	v_mov_b64_e32 v[58:59], v[42:43]
	v_mov_b64_e32 v[62:63], v[38:39]
	s_cbranch_vccnz .LBB0_5080
	s_cmp_lg_u32 s48, 0
	v_add_u32_e32 v6, s49, v178
	s_cbranch_scc0 .LBB0_5076
	v_add_u32_e32 v7, s48, v119
	v_add_u32_e32 v7, 0xffffff80, v7
	v_add_u32_e32 v8, 0x8ff, v6
	v_cndmask_b32_e64 v7, v8, v7, s[84:85]
	v_add_u32_e32 v22, s46, v7
	s_mov_b64 s[2:3], 0
	s_branch .LBB0_5077

.LBB0_5146:
	s_bitcmp1_b32 s55, 7
	s_cselect_b64 s[78:79], -1, 0
	s_and_b64 s[78:79], s[2:3], s[78:79]
	s_and_b64 s[78:79], s[78:79], exec
	s_cselect_b32 s37, s97, s39
	s_cselect_b32 s38, s96, s38
	v_mov_b32_e32 v87, s37
	s_ashr_i32 s37, s55, 1
	s_and_b32 s37, s37, 0xffffff80
	v_bitop3_b32 v89, s55, v188, v159 bitop3:0xc8
	v_or_b32_e32 v88, s55, v159
	v_or_b32_e32 v89, s37, v89
	v_or_b32_e32 v90, s54, v154
	v_mov_b32_e32 v86, s38
	v_cndmask_b32_e64 v88, v88, v89, s[2:3]
	v_mad_i64_i32 v[90:91], s[2:3], s36, v90, 0
	v_readlane_b32 s53, v242, 7
	v_ashrrev_i32_e32 v89, 31, v88
	v_lshl_add_u64 v[86:87], v[90:91], 2, v[86:87]
	s_mov_b32 m0, s53
	v_lshl_add_u64 v[86:87], v[88:89], 2, v[86:87]
	s_lshl_b32 s2, s36, 5
	s_mov_b32 s3, s31
	global_load_lds_dwordx4 v[86:87], off nt
	v_lshl_add_u64 v[86:87], v[86:87], 0, s[2:3]
	s_add_i32 m0, s53, 0x410
	v_readlane_b32 s36, v242, 34
	global_load_lds_dwordx4 v[86:87], off nt
	v_lshl_add_u64 v[86:87], v[86:87], 0, s[2:3]
	s_mov_b32 m0, s36
	v_readlane_b32 s36, v242, 35
	global_load_lds_dwordx4 v[86:87], off nt
	v_lshl_add_u64 v[86:87], v[86:87], 0, s[2:3]
	s_mov_b32 m0, s36
	v_readlane_b32 s36, v242, 38
	global_load_lds_dwordx4 v[86:87], off nt
	v_lshl_add_u64 v[86:87], v[86:87], 0, s[2:3]
	s_mov_b32 m0, s36
	v_readlane_b32 s36, v242, 24
	global_load_lds_dwordx4 v[86:87], off nt
	v_lshl_add_u64 v[86:87], v[86:87], 0, s[2:3]
	s_mov_b32 m0, s36
	v_readlane_b32 s36, v242, 27
	global_load_lds_dwordx4 v[86:87], off nt
	v_lshl_add_u64 v[86:87], v[86:87], 0, s[2:3]
	s_mov_b32 m0, s36
	s_nop 0
	global_load_lds_dwordx4 v[86:87], off nt
	v_lshl_add_u64 v[86:87], v[86:87], 0, s[2:3]
	v_readlane_b32 s2, v242, 29
	s_mov_b32 m0, s2
	s_nop 0
	global_load_lds_dwordx4 v[86:87], off nt
	s_mov_b32 s99, 1

	.amdhsa_kernel _Z4mega4Args
		.amdhsa_group_segment_fixed_size 0
		.amdhsa_private_segment_fixed_size 0
		.amdhsa_kernarg_size 512
		.amdhsa_user_sgpr_count 2
		.amdhsa_user_sgpr_dispatch_ptr 0
		.amdhsa_user_sgpr_queue_ptr 0
		.amdhsa_user_sgpr_kernarg_segment_ptr 1
		.amdhsa_user_sgpr_dispatch_id 0
		.amdhsa_user_sgpr_kernarg_preload_length 0
		.amdhsa_user_sgpr_kernarg_preload_offset 0
		.amdhsa_user_sgpr_private_segment_size 0
		.amdhsa_uses_dynamic_stack 0
		.amdhsa_enable_private_segment 0
		.amdhsa_system_sgpr_workgroup_id_x 1
		.amdhsa_system_sgpr_workgroup_id_y 0
		.amdhsa_system_sgpr_workgroup_id_z 0
		.amdhsa_system_sgpr_workgroup_info 0
		.amdhsa_system_vgpr_workitem_id 0
		.amdhsa_next_free_vgpr 244
		.amdhsa_next_free_sgpr 100
		.amdhsa_accum_offset 244
		.amdhsa_reserve_vcc 1
		.amdhsa_float_round_mode_32 0
		.amdhsa_float_round_mode_16_64 0
		.amdhsa_float_denorm_mode_32 3
		.amdhsa_float_denorm_mode_16_64 3
		.amdhsa_dx10_clamp 1
		.amdhsa_ieee_mode 1
		.amdhsa_fp16_overflow 0
		.amdhsa_tg_split 0
		.amdhsa_exception_fp_ieee_invalid_op 0
		.amdhsa_exception_fp_denorm_src 0
		.amdhsa_exception_fp_ieee_div_zero 0
		.amdhsa_exception_fp_ieee_overflow 0
		.amdhsa_exception_fp_ieee_underflow 0
		.amdhsa_exception_fp_ieee_inexact 0
		.amdhsa_exception_int_div_zero 0
	.end_amdhsa_kernel

amdhsa.kernels:
  - .agpr_count:     0
    .args:
      - .offset:         0
        .size:           256
        .value_kind:     by_value
      - .offset:         256
        .size:           4
        .value_kind:     hidden_block_count_x
      - .offset:         260
        .size:           4
        .value_kind:     hidden_block_count_y
      - .offset:         264
        .size:           4
        .value_kind:     hidden_block_count_z
      - .offset:         268
        .size:           2
        .value_kind:     hidden_group_size_x
      - .offset:         270
        .size:           2
        .value_kind:     hidden_group_size_y
      - .offset:         272
        .size:           2
        .value_kind:     hidden_group_size_z
      - .offset:         274
        .size:           2
        .value_kind:     hidden_remainder_x
      - .offset:         276
        .size:           2
        .value_kind:     hidden_remainder_y
      - .offset:         278
        .size:           2
        .value_kind:     hidden_remainder_z
      - .offset:         296
        .size:           8
        .value_kind:     hidden_global_offset_x
      - .offset:         304
        .size:           8
        .value_kind:     hidden_global_offset_y
      - .offset:         312
        .size:           8
        .value_kind:     hidden_global_offset_z
      - .offset:         320
        .size:           2
        .value_kind:     hidden_grid_dims
      - .offset:         376
        .size:           4
        .value_kind:     hidden_dynamic_lds_size
    .group_segment_fixed_size: 0
    .kernarg_segment_align: 8
    .kernarg_segment_size: 512
    .language:       OpenCL C
    .language_version:
      - 2
      - 0
    .max_flat_workgroup_size: 512
    .name:           _Z4mega4Args
    .private_segment_fixed_size: 0
    .sgpr_count:     106
    .sgpr_spill_count: 386
    .symbol:         _Z4mega4Args.kd
    .uniform_work_group_size: 1
    .uses_dynamic_stack: false
    .vgpr_count:     244
    .vgpr_spill_count: 0
    .wavefront_size: 64
